# dedicated weight conversion via LDS-DMA staging (lane-private), 2 slots per wave
# speedup vs baseline: 1.0029x; 1.0002x over previous
.Lcvt_site_398:
	s_waitcnt vmcnt(0) lgkmcnt(0)
	v_readlane_b32 s0, v254, 42
	v_readlane_b32 s1, v254, 43
	v_readlane_b32 s60, v254, 0
	v_readlane_b32 s61, v254, 41
	s_nop 3
	s_sub_u32 s0, s0, 0xd0
	s_subb_u32 s1, s1, 0
	s_load_dwordx2 s[10:11], s[0:1], 0x20
	s_load_dwordx2 s[12:13], s[0:1], 0x28
	s_load_dwordx2 s[14:15], s[0:1], 0x88
	s_load_dwordx2 s[28:29], s[0:1], 0x90
	s_load_dwordx2 s[38:39], s[0:1], 0x98
	s_load_dwordx2 s[44:45], s[0:1], 0xa0
	s_load_dwordx2 s[46:47], s[0:1], 0xa8
	s_load_dwordx2 s[48:49], s[0:1], 0xb8
	v_mbcnt_lo_u32_b32 v100, -1, 0
	v_mbcnt_hi_u32_b32 v100, -1, v100
	v_and_b32_e32 v96, 7, v100
	v_lshrrev_b32_e32 v97, 3, v100
	v_mov_b32_e32 v98, 0x43e00000
	s_mov_b32 s64, 0xc3e00000
	s_lshl_b32 s9, s60, 3
	s_add_u32 s9, s9, s61
	s_min_u32 s20, s74, 0x40
	s_lshl_b32 s20, s20, 4
	s_lshl_b32 s79, s61, 14
	s_add_u32 s69, s79, 0x2000
	v_lshlrev_b32_e32 v146, 4, v100
	v_add_u32_e32 v171, s69, v146
	v_add_u32_e32 v146, s79, v146
	s_waitcnt lgkmcnt(0)
	s_add_u32 s14, s14, 0x4000000
	s_addc_u32 s15, s15, 0
	s_add_u32 s28, s28, 0x4000000
	s_addc_u32 s29, s29, 0
	s_add_u32 s38, s38, 0x4000000
	s_addc_u32 s39, s39, 0
	s_add_u32 s44, s44, 0x400000
	s_addc_u32 s45, s45, 0
	s_add_u32 s46, s46, 0x100000
	s_addc_u32 s47, s47, 0
	s_add_u32 s48, s48, 0x2bd00000
	s_addc_u32 s49, s49, 0
	s_lshl_b32 s32, s9, 1
	s_mov_b32 s41, 0
	s_cmp_lt_u32 s32, 0x6780
	s_cbranch_scc0 .Lcv398_drain
	s_add_u32 s43, s32, 0
	s_cmp_lt_u32 s43, 0x300
	s_cbranch_scc0 .Lcv398_d0_b
	s_mul_i32 s58, s43, 0xaaab
	s_lshr_b32 s58, s58, 21
	s_mul_i32 s59, s58, 48
	s_sub_u32 s59, s43, s59
	s_mul_i32 s60, s58, 0x60000
	s_mul_i32 s81, s59, 0x80
	s_add_u32 s60, s60, s81
	s_add_u32 s2, s10, s60
	s_addc_u32 s3, s11, 0
	s_mov_b32 s63, 0x1800
	s_mul_i32 s61, s59, 0x8000
	s_mul_i32 s81, s58, 0x40
	s_add_u32 s61, s61, s81
	s_add_u32 s61, s61, 0x800000
	s_add_u32 s50, s48, s61
	s_addc_u32 s51, s49, 0
	s_mov_b32 s65, 0x400
	s_mov_b32 s71, 0x44000000
	s_branch .Lcv398_d0_ld

.Lcv398_d0_ld:
	s_lshl_b32 s60, s63, 3
	v_mul_lo_u32 v0, v96, s60
	v_lshl_add_u32 v0, v97, 4, v0
	v_add_u32_e32 v4, s63, v0
	v_add_u32_e32 v10, s63, v4
	v_add_u32_e32 v11, s63, v10
	v_add_u32_e32 v12, s63, v11
	v_add_u32_e32 v19, s63, v12
	v_add_u32_e32 v24, s63, v19
	v_add_u32_e32 v25, s63, v24
	s_add_i32 m0, s79, 0x0
	s_nop 0
	global_load_lds_dwordx4 v0, s[2:3] nt
	s_add_i32 m0, s79, 0x400
	s_nop 0
	global_load_lds_dwordx4 v4, s[2:3] nt
	s_add_i32 m0, s79, 0x800
	s_nop 0
	global_load_lds_dwordx4 v10, s[2:3] nt
	s_add_i32 m0, s79, 0xc00
	s_nop 0
	global_load_lds_dwordx4 v11, s[2:3] nt
	s_add_i32 m0, s79, 0x1000
	s_nop 0
	global_load_lds_dwordx4 v12, s[2:3] nt
	s_add_i32 m0, s79, 0x1400
	s_nop 0
	global_load_lds_dwordx4 v19, s[2:3] nt
	s_add_i32 m0, s79, 0x1800
	s_nop 0
	global_load_lds_dwordx4 v24, s[2:3] nt
	s_add_i32 m0, s79, 0x1c00
	s_nop 0
	global_load_lds_dwordx4 v25, s[2:3] nt
	s_mov_b32 s41, 1
	s_cmp_lt_u32 s32, 0x6780
	s_cbranch_scc0 .Lcv398_drain
	s_add_u32 s43, s32, 1
	s_cmp_lt_u32 s43, 0x300
	s_cbranch_scc0 .Lcv398_d1_b
	s_mul_i32 s58, s43, 0xaaab
	s_lshr_b32 s58, s58, 21
	s_mul_i32 s59, s58, 48
	s_sub_u32 s59, s43, s59
	s_mul_i32 s60, s58, 0x60000
	s_mul_i32 s81, s59, 0x80
	s_add_u32 s60, s60, s81
	s_add_u32 s2, s10, s60
	s_addc_u32 s3, s11, 0
	s_mov_b32 s63, 0x1800
	s_mul_i32 s61, s59, 0x8000
	s_mul_i32 s81, s58, 0x40
	s_add_u32 s61, s61, s81
	s_add_u32 s61, s61, 0x800000
	s_add_u32 s52, s48, s61
	s_addc_u32 s53, s49, 0
	s_mov_b32 s66, 0x400
	s_mov_b32 s75, 0x44000000
	s_branch .Lcv398_d1_ld

.Lcv398_d1_ld:
	s_lshl_b32 s60, s63, 3
	v_mul_lo_u32 v0, v96, s60
	v_lshl_add_u32 v0, v97, 4, v0
	v_add_u32_e32 v4, s63, v0
	v_add_u32_e32 v10, s63, v4
	v_add_u32_e32 v11, s63, v10
	v_add_u32_e32 v12, s63, v11
	v_add_u32_e32 v19, s63, v12
	v_add_u32_e32 v24, s63, v19
	v_add_u32_e32 v25, s63, v24
	s_add_i32 m0, s69, 0x0
	s_nop 0
	global_load_lds_dwordx4 v0, s[2:3] nt
	s_add_i32 m0, s69, 0x400
	s_nop 0
	global_load_lds_dwordx4 v4, s[2:3] nt
	s_add_i32 m0, s69, 0x800
	s_nop 0
	global_load_lds_dwordx4 v10, s[2:3] nt
	s_add_i32 m0, s69, 0xc00
	s_nop 0
	global_load_lds_dwordx4 v11, s[2:3] nt
	s_add_i32 m0, s69, 0x1000
	s_nop 0
	global_load_lds_dwordx4 v12, s[2:3] nt
	s_add_i32 m0, s69, 0x1400
	s_nop 0
	global_load_lds_dwordx4 v19, s[2:3] nt
	s_add_i32 m0, s69, 0x1800
	s_nop 0
	global_load_lds_dwordx4 v24, s[2:3] nt
	s_add_i32 m0, s69, 0x1c00
	s_nop 0
	global_load_lds_dwordx4 v25, s[2:3] nt
	s_mov_b32 s41, 2
	s_add_u32 s32, s32, s20
.Lcv398_loop:
	s_cmp_lt_u32 s32, 0x6780
	s_cbranch_scc0 .Lcv398_drain0
	s_waitcnt vmcnt(8)
	ds_read_b128 v[34:37], v146 offset:0
	ds_read_b128 v[38:41], v146 offset:1024
	ds_read_b128 v[42:45], v146 offset:2048
	ds_read_b128 v[46:49], v146 offset:3072
	ds_read_b128 v[50:53], v146 offset:4096
	ds_read_b128 v[54:57], v146 offset:5120
	ds_read_b128 v[58:61], v146 offset:6144
	ds_read_b128 v[62:65], v146 offset:7168
	s_waitcnt lgkmcnt(0)
	s_mov_b64 s[2:3], s[50:51]
	s_lshl_b32 s60, s65, 2
	v_mul_lo_u32 v27, v97, s60
	s_cmp_eq_u32 s71, 0
	s_cbranch_scc1 .Lcv398_p2_bf
	v_lshl_add_u32 v27, v96, 3, v27
	v_add_u32_e32 v32, s65, v27
	v_add_u32_e32 v92, s65, v32
	v_add_u32_e32 v94, s65, v92
	v_mul_f32_e32 v34, s71, v34
	v_mul_f32_e32 v35, s71, v35
	v_mul_f32_e32 v36, s71, v36
	v_mul_f32_e32 v37, s71, v37
	v_mul_f32_e32 v38, s71, v38
	v_mul_f32_e32 v39, s71, v39
	v_mul_f32_e32 v40, s71, v40
	v_mul_f32_e32 v41, s71, v41
	v_mul_f32_e32 v42, s71, v42
	v_mul_f32_e32 v43, s71, v43
	v_mul_f32_e32 v44, s71, v44
	v_mul_f32_e32 v45, s71, v45
	v_mul_f32_e32 v46, s71, v46
	v_mul_f32_e32 v47, s71, v47
	v_mul_f32_e32 v48, s71, v48
	v_mul_f32_e32 v49, s71, v49
	v_mul_f32_e32 v50, s71, v50
	v_mul_f32_e32 v51, s71, v51
	v_mul_f32_e32 v52, s71, v52
	v_mul_f32_e32 v53, s71, v53
	v_mul_f32_e32 v54, s71, v54
	v_mul_f32_e32 v55, s71, v55
	v_mul_f32_e32 v56, s71, v56
	v_mul_f32_e32 v57, s71, v57
	v_mul_f32_e32 v58, s71, v58
	v_mul_f32_e32 v59, s71, v59
	v_mul_f32_e32 v60, s71, v60
	v_mul_f32_e32 v61, s71, v61
	v_mul_f32_e32 v62, s71, v62
	v_mul_f32_e32 v63, s71, v63
	v_mul_f32_e32 v64, s71, v64
	v_mul_f32_e32 v65, s71, v65
	v_med3_f32 v34, v34, s64, v98
	v_med3_f32 v35, v35, s64, v98
	v_med3_f32 v36, v36, s64, v98
	v_med3_f32 v37, v37, s64, v98
	v_med3_f32 v38, v38, s64, v98
	v_med3_f32 v39, v39, s64, v98
	v_med3_f32 v40, v40, s64, v98
	v_med3_f32 v41, v41, s64, v98
	v_med3_f32 v42, v42, s64, v98
	v_med3_f32 v43, v43, s64, v98
	v_med3_f32 v44, v44, s64, v98
	v_med3_f32 v45, v45, s64, v98
	v_med3_f32 v46, v46, s64, v98
	v_med3_f32 v47, v47, s64, v98
	v_med3_f32 v48, v48, s64, v98
	v_med3_f32 v49, v49, s64, v98
	v_med3_f32 v50, v50, s64, v98
	v_med3_f32 v51, v51, s64, v98
	v_med3_f32 v52, v52, s64, v98
	v_med3_f32 v53, v53, s64, v98
	v_med3_f32 v54, v54, s64, v98
	v_med3_f32 v55, v55, s64, v98
	v_med3_f32 v56, v56, s64, v98
	v_med3_f32 v57, v57, s64, v98
	v_med3_f32 v58, v58, s64, v98
	v_med3_f32 v59, v59, s64, v98
	v_med3_f32 v60, v60, s64, v98
	v_med3_f32 v61, v61, s64, v98
	v_med3_f32 v62, v62, s64, v98
	v_med3_f32 v63, v63, s64, v98
	v_med3_f32 v64, v64, s64, v98
	v_med3_f32 v65, v65, s64, v98
	v_cvt_pk_fp8_f32 v148, v34, v38
	v_cvt_pk_fp8_f32 v149, v50, v54
	v_cvt_pk_fp8_f32 v152, v35, v39
	v_cvt_pk_fp8_f32 v153, v51, v55
	v_cvt_pk_fp8_f32 v158, v36, v40
	v_cvt_pk_fp8_f32 v159, v52, v56
	v_cvt_pk_fp8_f32 v196, v37, v41
	v_cvt_pk_fp8_f32 v197, v53, v57
	v_cvt_pk_fp8_f32 v148, v42, v46 op_sel:[0,0,1]
	v_cvt_pk_fp8_f32 v149, v58, v62 op_sel:[0,0,1]
	v_cvt_pk_fp8_f32 v152, v43, v47 op_sel:[0,0,1]
	v_cvt_pk_fp8_f32 v153, v59, v63 op_sel:[0,0,1]
	v_cvt_pk_fp8_f32 v158, v44, v48 op_sel:[0,0,1]
	v_cvt_pk_fp8_f32 v159, v60, v64 op_sel:[0,0,1]
	v_cvt_pk_fp8_f32 v196, v45, v49 op_sel:[0,0,1]
	v_cvt_pk_fp8_f32 v197, v61, v65 op_sel:[0,0,1]
	s_nop 1
	global_store_dwordx2 v27, v[148:149], s[50:51]
	global_store_dwordx2 v32, v[152:153], s[50:51]
	global_store_dwordx2 v92, v[158:159], s[50:51]
	global_store_dwordx2 v94, v[196:197], s[50:51]
	s_branch .Lcv398_p2_end

.Lcv398_d3_ld:
	s_lshl_b32 s60, s63, 3
	v_mul_lo_u32 v0, v96, s60
	v_lshl_add_u32 v0, v97, 4, v0
	v_add_u32_e32 v4, s63, v0
	v_add_u32_e32 v10, s63, v4
	v_add_u32_e32 v11, s63, v10
	v_add_u32_e32 v12, s63, v11
	v_add_u32_e32 v19, s63, v12
	v_add_u32_e32 v24, s63, v19
	v_add_u32_e32 v25, s63, v24
	s_add_i32 m0, s79, 0x0
	s_nop 0
	global_load_lds_dwordx4 v0, s[2:3] nt
	s_add_i32 m0, s79, 0x400
	s_nop 0
	global_load_lds_dwordx4 v4, s[2:3] nt
	s_add_i32 m0, s79, 0x800
	s_nop 0
	global_load_lds_dwordx4 v10, s[2:3] nt
	s_add_i32 m0, s79, 0xc00
	s_nop 0
	global_load_lds_dwordx4 v11, s[2:3] nt
	s_add_i32 m0, s79, 0x1000
	s_nop 0
	global_load_lds_dwordx4 v12, s[2:3] nt
	s_add_i32 m0, s79, 0x1400
	s_nop 0
	global_load_lds_dwordx4 v19, s[2:3] nt
	s_add_i32 m0, s79, 0x1800
	s_nop 0
	global_load_lds_dwordx4 v24, s[2:3] nt
	s_add_i32 m0, s79, 0x1c00
	s_nop 0
	global_load_lds_dwordx4 v25, s[2:3] nt
	s_cmp_lt_u32 s32, 0x6780
	s_cbranch_scc0 .Lcv398_drain1
	s_waitcnt vmcnt(8)
	ds_read_b128 v[34:37], v171 offset:0
	ds_read_b128 v[38:41], v171 offset:1024
	ds_read_b128 v[42:45], v171 offset:2048
	ds_read_b128 v[46:49], v171 offset:3072
	ds_read_b128 v[50:53], v171 offset:4096
	ds_read_b128 v[54:57], v171 offset:5120
	ds_read_b128 v[58:61], v171 offset:6144
	ds_read_b128 v[62:65], v171 offset:7168
	s_waitcnt lgkmcnt(0)
	s_mov_b64 s[2:3], s[52:53]
	s_lshl_b32 s60, s66, 2
	v_mul_lo_u32 v27, v97, s60
	s_cmp_eq_u32 s75, 0
	s_cbranch_scc1 .Lcv398_p4_bf
	v_lshl_add_u32 v27, v96, 3, v27
	v_add_u32_e32 v32, s66, v27
	v_add_u32_e32 v92, s66, v32
	v_add_u32_e32 v94, s66, v92
	v_mul_f32_e32 v34, s75, v34
	v_mul_f32_e32 v35, s75, v35
	v_mul_f32_e32 v36, s75, v36
	v_mul_f32_e32 v37, s75, v37
	v_mul_f32_e32 v38, s75, v38
	v_mul_f32_e32 v39, s75, v39
	v_mul_f32_e32 v40, s75, v40
	v_mul_f32_e32 v41, s75, v41
	v_mul_f32_e32 v42, s75, v42
	v_mul_f32_e32 v43, s75, v43
	v_mul_f32_e32 v44, s75, v44
	v_mul_f32_e32 v45, s75, v45
	v_mul_f32_e32 v46, s75, v46
	v_mul_f32_e32 v47, s75, v47
	v_mul_f32_e32 v48, s75, v48
	v_mul_f32_e32 v49, s75, v49
	v_mul_f32_e32 v50, s75, v50
	v_mul_f32_e32 v51, s75, v51
	v_mul_f32_e32 v52, s75, v52
	v_mul_f32_e32 v53, s75, v53
	v_mul_f32_e32 v54, s75, v54
	v_mul_f32_e32 v55, s75, v55
	v_mul_f32_e32 v56, s75, v56
	v_mul_f32_e32 v57, s75, v57
	v_mul_f32_e32 v58, s75, v58
	v_mul_f32_e32 v59, s75, v59
	v_mul_f32_e32 v60, s75, v60
	v_mul_f32_e32 v61, s75, v61
	v_mul_f32_e32 v62, s75, v62
	v_mul_f32_e32 v63, s75, v63
	v_mul_f32_e32 v64, s75, v64
	v_mul_f32_e32 v65, s75, v65
	v_med3_f32 v34, v34, s64, v98
	v_med3_f32 v35, v35, s64, v98
	v_med3_f32 v36, v36, s64, v98
	v_med3_f32 v37, v37, s64, v98
	v_med3_f32 v38, v38, s64, v98
	v_med3_f32 v39, v39, s64, v98
	v_med3_f32 v40, v40, s64, v98
	v_med3_f32 v41, v41, s64, v98
	v_med3_f32 v42, v42, s64, v98
	v_med3_f32 v43, v43, s64, v98
	v_med3_f32 v44, v44, s64, v98
	v_med3_f32 v45, v45, s64, v98
	v_med3_f32 v46, v46, s64, v98
	v_med3_f32 v47, v47, s64, v98
	v_med3_f32 v48, v48, s64, v98
	v_med3_f32 v49, v49, s64, v98
	v_med3_f32 v50, v50, s64, v98
	v_med3_f32 v51, v51, s64, v98
	v_med3_f32 v52, v52, s64, v98
	v_med3_f32 v53, v53, s64, v98
	v_med3_f32 v54, v54, s64, v98
	v_med3_f32 v55, v55, s64, v98
	v_med3_f32 v56, v56, s64, v98
	v_med3_f32 v57, v57, s64, v98
	v_med3_f32 v58, v58, s64, v98
	v_med3_f32 v59, v59, s64, v98
	v_med3_f32 v60, v60, s64, v98
	v_med3_f32 v61, v61, s64, v98
	v_med3_f32 v62, v62, s64, v98
	v_med3_f32 v63, v63, s64, v98
	v_med3_f32 v64, v64, s64, v98
	v_med3_f32 v65, v65, s64, v98
	v_cvt_pk_fp8_f32 v148, v34, v38
	v_cvt_pk_fp8_f32 v149, v50, v54
	v_cvt_pk_fp8_f32 v152, v35, v39
	v_cvt_pk_fp8_f32 v153, v51, v55
	v_cvt_pk_fp8_f32 v158, v36, v40
	v_cvt_pk_fp8_f32 v159, v52, v56
	v_cvt_pk_fp8_f32 v196, v37, v41
	v_cvt_pk_fp8_f32 v197, v53, v57
	v_cvt_pk_fp8_f32 v148, v42, v46 op_sel:[0,0,1]
	v_cvt_pk_fp8_f32 v149, v58, v62 op_sel:[0,0,1]
	v_cvt_pk_fp8_f32 v152, v43, v47 op_sel:[0,0,1]
	v_cvt_pk_fp8_f32 v153, v59, v63 op_sel:[0,0,1]
	v_cvt_pk_fp8_f32 v158, v44, v48 op_sel:[0,0,1]
	v_cvt_pk_fp8_f32 v159, v60, v64 op_sel:[0,0,1]
	v_cvt_pk_fp8_f32 v196, v45, v49 op_sel:[0,0,1]
	v_cvt_pk_fp8_f32 v197, v61, v65 op_sel:[0,0,1]
	s_nop 1
	global_store_dwordx2 v27, v[148:149], s[52:53]
	global_store_dwordx2 v32, v[152:153], s[52:53]
	global_store_dwordx2 v92, v[158:159], s[52:53]
	global_store_dwordx2 v94, v[196:197], s[52:53]
	s_branch .Lcv398_p4_end
.Lcv398_p4_bf:
	v_lshl_add_u32 v27, v96, 4, v27
	v_add_u32_e32 v32, s66, v27
	v_add_u32_e32 v92, s66, v32
	v_add_u32_e32 v94, s66, v92
	v_cvt_pk_bf16_f32 v148, v34, v38
	v_cvt_pk_bf16_f32 v149, v42, v46
	v_cvt_pk_bf16_f32 v202, v50, v54
	v_cvt_pk_bf16_f32 v203, v58, v62
	v_cvt_pk_bf16_f32 v152, v35, v39
	v_cvt_pk_bf16_f32 v153, v43, v47
	v_cvt_pk_bf16_f32 v208, v51, v55
	v_cvt_pk_bf16_f32 v209, v59, v63
	v_cvt_pk_bf16_f32 v158, v36, v40
	v_cvt_pk_bf16_f32 v159, v44, v48
	v_cvt_pk_bf16_f32 v220, v52, v56
	v_cvt_pk_bf16_f32 v221, v60, v64
	v_cvt_pk_bf16_f32 v196, v37, v41
	v_cvt_pk_bf16_f32 v197, v45, v49
	v_cvt_pk_bf16_f32 v226, v53, v57
	v_cvt_pk_bf16_f32 v227, v61, v65
	s_nop 1
	global_store_dwordx2 v27, v[148:149], s[52:53]
	global_store_dwordx2 v27, v[202:203], s[52:53] offset:8
	global_store_dwordx2 v32, v[152:153], s[52:53]
	global_store_dwordx2 v32, v[208:209], s[52:53] offset:8
	global_store_dwordx2 v92, v[158:159], s[52:53]
	global_store_dwordx2 v92, v[220:221], s[52:53] offset:8
	global_store_dwordx2 v94, v[196:197], s[52:53]
	global_store_dwordx2 v94, v[226:227], s[52:53] offset:8

.Lcv398_d5_ld:
	s_lshl_b32 s60, s63, 3
	v_mul_lo_u32 v0, v96, s60
	v_lshl_add_u32 v0, v97, 4, v0
	v_add_u32_e32 v4, s63, v0
	v_add_u32_e32 v10, s63, v4
	v_add_u32_e32 v11, s63, v10
	v_add_u32_e32 v12, s63, v11
	v_add_u32_e32 v19, s63, v12
	v_add_u32_e32 v24, s63, v19
	v_add_u32_e32 v25, s63, v24
	s_add_i32 m0, s69, 0x0
	s_nop 0
	global_load_lds_dwordx4 v0, s[2:3] nt
	s_add_i32 m0, s69, 0x400
	s_nop 0
	global_load_lds_dwordx4 v4, s[2:3] nt
	s_add_i32 m0, s69, 0x800
	s_nop 0
	global_load_lds_dwordx4 v10, s[2:3] nt
	s_add_i32 m0, s69, 0xc00
	s_nop 0
	global_load_lds_dwordx4 v11, s[2:3] nt
	s_add_i32 m0, s69, 0x1000
	s_nop 0
	global_load_lds_dwordx4 v12, s[2:3] nt
	s_add_i32 m0, s69, 0x1400
	s_nop 0
	global_load_lds_dwordx4 v19, s[2:3] nt
	s_add_i32 m0, s69, 0x1800
	s_nop 0
	global_load_lds_dwordx4 v24, s[2:3] nt
	s_add_i32 m0, s69, 0x1c00
	s_nop 0
	global_load_lds_dwordx4 v25, s[2:3] nt
	s_add_u32 s32, s32, s20
	s_branch .Lcv398_loop
.Lcv398_drain0:
	s_waitcnt vmcnt(0)
	ds_read_b128 v[34:37], v146 offset:0
	ds_read_b128 v[38:41], v146 offset:1024
	ds_read_b128 v[42:45], v146 offset:2048
	ds_read_b128 v[46:49], v146 offset:3072
	ds_read_b128 v[50:53], v146 offset:4096
	ds_read_b128 v[54:57], v146 offset:5120
	ds_read_b128 v[58:61], v146 offset:6144
	ds_read_b128 v[62:65], v146 offset:7168
	s_waitcnt lgkmcnt(0)
	s_lshl_b32 s60, s65, 2
	v_mul_lo_u32 v27, v97, s60
	s_cmp_eq_u32 s71, 0
	s_cbranch_scc1 .Lcv398_p6_bf
	v_lshl_add_u32 v27, v96, 3, v27
	v_add_u32_e32 v32, s65, v27
	v_add_u32_e32 v92, s65, v32
	v_add_u32_e32 v94, s65, v92
	v_mul_f32_e32 v34, s71, v34
	v_mul_f32_e32 v35, s71, v35
	v_mul_f32_e32 v36, s71, v36
	v_mul_f32_e32 v37, s71, v37
	v_mul_f32_e32 v38, s71, v38
	v_mul_f32_e32 v39, s71, v39
	v_mul_f32_e32 v40, s71, v40
	v_mul_f32_e32 v41, s71, v41
	v_mul_f32_e32 v42, s71, v42
	v_mul_f32_e32 v43, s71, v43
	v_mul_f32_e32 v44, s71, v44
	v_mul_f32_e32 v45, s71, v45
	v_mul_f32_e32 v46, s71, v46
	v_mul_f32_e32 v47, s71, v47
	v_mul_f32_e32 v48, s71, v48
	v_mul_f32_e32 v49, s71, v49
	v_mul_f32_e32 v50, s71, v50
	v_mul_f32_e32 v51, s71, v51
	v_mul_f32_e32 v52, s71, v52
	v_mul_f32_e32 v53, s71, v53
	v_mul_f32_e32 v54, s71, v54
	v_mul_f32_e32 v55, s71, v55
	v_mul_f32_e32 v56, s71, v56
	v_mul_f32_e32 v57, s71, v57
	v_mul_f32_e32 v58, s71, v58
	v_mul_f32_e32 v59, s71, v59
	v_mul_f32_e32 v60, s71, v60
	v_mul_f32_e32 v61, s71, v61
	v_mul_f32_e32 v62, s71, v62
	v_mul_f32_e32 v63, s71, v63
	v_mul_f32_e32 v64, s71, v64
	v_mul_f32_e32 v65, s71, v65
	v_med3_f32 v34, v34, s64, v98
	v_med3_f32 v35, v35, s64, v98
	v_med3_f32 v36, v36, s64, v98
	v_med3_f32 v37, v37, s64, v98
	v_med3_f32 v38, v38, s64, v98
	v_med3_f32 v39, v39, s64, v98
	v_med3_f32 v40, v40, s64, v98
	v_med3_f32 v41, v41, s64, v98
	v_med3_f32 v42, v42, s64, v98
	v_med3_f32 v43, v43, s64, v98
	v_med3_f32 v44, v44, s64, v98
	v_med3_f32 v45, v45, s64, v98
	v_med3_f32 v46, v46, s64, v98
	v_med3_f32 v47, v47, s64, v98
	v_med3_f32 v48, v48, s64, v98
	v_med3_f32 v49, v49, s64, v98
	v_med3_f32 v50, v50, s64, v98
	v_med3_f32 v51, v51, s64, v98
	v_med3_f32 v52, v52, s64, v98
	v_med3_f32 v53, v53, s64, v98
	v_med3_f32 v54, v54, s64, v98
	v_med3_f32 v55, v55, s64, v98
	v_med3_f32 v56, v56, s64, v98
	v_med3_f32 v57, v57, s64, v98
	v_med3_f32 v58, v58, s64, v98
	v_med3_f32 v59, v59, s64, v98
	v_med3_f32 v60, v60, s64, v98
	v_med3_f32 v61, v61, s64, v98
	v_med3_f32 v62, v62, s64, v98
	v_med3_f32 v63, v63, s64, v98
	v_med3_f32 v64, v64, s64, v98
	v_med3_f32 v65, v65, s64, v98
	v_cvt_pk_fp8_f32 v148, v34, v38
	v_cvt_pk_fp8_f32 v149, v50, v54
	v_cvt_pk_fp8_f32 v152, v35, v39
	v_cvt_pk_fp8_f32 v153, v51, v55
	v_cvt_pk_fp8_f32 v158, v36, v40
	v_cvt_pk_fp8_f32 v159, v52, v56
	v_cvt_pk_fp8_f32 v196, v37, v41
	v_cvt_pk_fp8_f32 v197, v53, v57
	v_cvt_pk_fp8_f32 v148, v42, v46 op_sel:[0,0,1]
	v_cvt_pk_fp8_f32 v149, v58, v62 op_sel:[0,0,1]
	v_cvt_pk_fp8_f32 v152, v43, v47 op_sel:[0,0,1]
	v_cvt_pk_fp8_f32 v153, v59, v63 op_sel:[0,0,1]
	v_cvt_pk_fp8_f32 v158, v44, v48 op_sel:[0,0,1]
	v_cvt_pk_fp8_f32 v159, v60, v64 op_sel:[0,0,1]
	v_cvt_pk_fp8_f32 v196, v45, v49 op_sel:[0,0,1]
	v_cvt_pk_fp8_f32 v197, v61, v65 op_sel:[0,0,1]
	s_nop 1
	global_store_dwordx2 v27, v[148:149], s[50:51]
	global_store_dwordx2 v32, v[152:153], s[50:51]
	global_store_dwordx2 v92, v[158:159], s[50:51]
	global_store_dwordx2 v94, v[196:197], s[50:51]
	s_branch .Lcv398_p6_end

.Lcv398_p6_end:
	ds_read_b128 v[34:37], v171 offset:0
	ds_read_b128 v[38:41], v171 offset:1024
	ds_read_b128 v[42:45], v171 offset:2048
	ds_read_b128 v[46:49], v171 offset:3072
	ds_read_b128 v[50:53], v171 offset:4096
	ds_read_b128 v[54:57], v171 offset:5120
	ds_read_b128 v[58:61], v171 offset:6144
	ds_read_b128 v[62:65], v171 offset:7168
	s_waitcnt lgkmcnt(0)
	s_lshl_b32 s60, s66, 2
	v_mul_lo_u32 v27, v97, s60
	s_cmp_eq_u32 s75, 0
	s_cbranch_scc1 .Lcv398_p7_bf
	v_lshl_add_u32 v27, v96, 3, v27
	v_add_u32_e32 v32, s66, v27
	v_add_u32_e32 v92, s66, v32
	v_add_u32_e32 v94, s66, v92
	v_mul_f32_e32 v34, s75, v34
	v_mul_f32_e32 v35, s75, v35
	v_mul_f32_e32 v36, s75, v36
	v_mul_f32_e32 v37, s75, v37
	v_mul_f32_e32 v38, s75, v38
	v_mul_f32_e32 v39, s75, v39
	v_mul_f32_e32 v40, s75, v40
	v_mul_f32_e32 v41, s75, v41
	v_mul_f32_e32 v42, s75, v42
	v_mul_f32_e32 v43, s75, v43
	v_mul_f32_e32 v44, s75, v44
	v_mul_f32_e32 v45, s75, v45
	v_mul_f32_e32 v46, s75, v46
	v_mul_f32_e32 v47, s75, v47
	v_mul_f32_e32 v48, s75, v48
	v_mul_f32_e32 v49, s75, v49
	v_mul_f32_e32 v50, s75, v50
	v_mul_f32_e32 v51, s75, v51
	v_mul_f32_e32 v52, s75, v52
	v_mul_f32_e32 v53, s75, v53
	v_mul_f32_e32 v54, s75, v54
	v_mul_f32_e32 v55, s75, v55
	v_mul_f32_e32 v56, s75, v56
	v_mul_f32_e32 v57, s75, v57
	v_mul_f32_e32 v58, s75, v58
	v_mul_f32_e32 v59, s75, v59
	v_mul_f32_e32 v60, s75, v60
	v_mul_f32_e32 v61, s75, v61
	v_mul_f32_e32 v62, s75, v62
	v_mul_f32_e32 v63, s75, v63
	v_mul_f32_e32 v64, s75, v64
	v_mul_f32_e32 v65, s75, v65
	v_med3_f32 v34, v34, s64, v98
	v_med3_f32 v35, v35, s64, v98
	v_med3_f32 v36, v36, s64, v98
	v_med3_f32 v37, v37, s64, v98
	v_med3_f32 v38, v38, s64, v98
	v_med3_f32 v39, v39, s64, v98
	v_med3_f32 v40, v40, s64, v98
	v_med3_f32 v41, v41, s64, v98
	v_med3_f32 v42, v42, s64, v98
	v_med3_f32 v43, v43, s64, v98
	v_med3_f32 v44, v44, s64, v98
	v_med3_f32 v45, v45, s64, v98
	v_med3_f32 v46, v46, s64, v98
	v_med3_f32 v47, v47, s64, v98
	v_med3_f32 v48, v48, s64, v98
	v_med3_f32 v49, v49, s64, v98
	v_med3_f32 v50, v50, s64, v98
	v_med3_f32 v51, v51, s64, v98
	v_med3_f32 v52, v52, s64, v98
	v_med3_f32 v53, v53, s64, v98
	v_med3_f32 v54, v54, s64, v98
	v_med3_f32 v55, v55, s64, v98
	v_med3_f32 v56, v56, s64, v98
	v_med3_f32 v57, v57, s64, v98
	v_med3_f32 v58, v58, s64, v98
	v_med3_f32 v59, v59, s64, v98
	v_med3_f32 v60, v60, s64, v98
	v_med3_f32 v61, v61, s64, v98
	v_med3_f32 v62, v62, s64, v98
	v_med3_f32 v63, v63, s64, v98
	v_med3_f32 v64, v64, s64, v98
	v_med3_f32 v65, v65, s64, v98
	v_cvt_pk_fp8_f32 v148, v34, v38
	v_cvt_pk_fp8_f32 v149, v50, v54
	v_cvt_pk_fp8_f32 v152, v35, v39
	v_cvt_pk_fp8_f32 v153, v51, v55
	v_cvt_pk_fp8_f32 v158, v36, v40
	v_cvt_pk_fp8_f32 v159, v52, v56
	v_cvt_pk_fp8_f32 v196, v37, v41
	v_cvt_pk_fp8_f32 v197, v53, v57
	v_cvt_pk_fp8_f32 v148, v42, v46 op_sel:[0,0,1]
	v_cvt_pk_fp8_f32 v149, v58, v62 op_sel:[0,0,1]
	v_cvt_pk_fp8_f32 v152, v43, v47 op_sel:[0,0,1]
	v_cvt_pk_fp8_f32 v153, v59, v63 op_sel:[0,0,1]
	v_cvt_pk_fp8_f32 v158, v44, v48 op_sel:[0,0,1]
	v_cvt_pk_fp8_f32 v159, v60, v64 op_sel:[0,0,1]
	v_cvt_pk_fp8_f32 v196, v45, v49 op_sel:[0,0,1]
	v_cvt_pk_fp8_f32 v197, v61, v65 op_sel:[0,0,1]
	s_nop 1
	global_store_dwordx2 v27, v[148:149], s[52:53]
	global_store_dwordx2 v32, v[152:153], s[52:53]
	global_store_dwordx2 v92, v[158:159], s[52:53]
	global_store_dwordx2 v94, v[196:197], s[52:53]
	s_branch .Lcv398_p7_end

.Lcv398_drain1:
	s_waitcnt vmcnt(0)
	ds_read_b128 v[34:37], v171 offset:0
	ds_read_b128 v[38:41], v171 offset:1024
	ds_read_b128 v[42:45], v171 offset:2048
	ds_read_b128 v[46:49], v171 offset:3072
	ds_read_b128 v[50:53], v171 offset:4096
	ds_read_b128 v[54:57], v171 offset:5120
	ds_read_b128 v[58:61], v171 offset:6144
	ds_read_b128 v[62:65], v171 offset:7168
	s_waitcnt lgkmcnt(0)
	s_lshl_b32 s60, s66, 2
	v_mul_lo_u32 v27, v97, s60
	s_cmp_eq_u32 s75, 0
	s_cbranch_scc1 .Lcv398_p8_bf
	v_lshl_add_u32 v27, v96, 3, v27
	v_add_u32_e32 v32, s66, v27
	v_add_u32_e32 v92, s66, v32
	v_add_u32_e32 v94, s66, v92
	v_mul_f32_e32 v34, s75, v34
	v_mul_f32_e32 v35, s75, v35
	v_mul_f32_e32 v36, s75, v36
	v_mul_f32_e32 v37, s75, v37
	v_mul_f32_e32 v38, s75, v38
	v_mul_f32_e32 v39, s75, v39
	v_mul_f32_e32 v40, s75, v40
	v_mul_f32_e32 v41, s75, v41
	v_mul_f32_e32 v42, s75, v42
	v_mul_f32_e32 v43, s75, v43
	v_mul_f32_e32 v44, s75, v44
	v_mul_f32_e32 v45, s75, v45
	v_mul_f32_e32 v46, s75, v46
	v_mul_f32_e32 v47, s75, v47
	v_mul_f32_e32 v48, s75, v48
	v_mul_f32_e32 v49, s75, v49
	v_mul_f32_e32 v50, s75, v50
	v_mul_f32_e32 v51, s75, v51
	v_mul_f32_e32 v52, s75, v52
	v_mul_f32_e32 v53, s75, v53
	v_mul_f32_e32 v54, s75, v54
	v_mul_f32_e32 v55, s75, v55
	v_mul_f32_e32 v56, s75, v56
	v_mul_f32_e32 v57, s75, v57
	v_mul_f32_e32 v58, s75, v58
	v_mul_f32_e32 v59, s75, v59
	v_mul_f32_e32 v60, s75, v60
	v_mul_f32_e32 v61, s75, v61
	v_mul_f32_e32 v62, s75, v62
	v_mul_f32_e32 v63, s75, v63
	v_mul_f32_e32 v64, s75, v64
	v_mul_f32_e32 v65, s75, v65
	v_med3_f32 v34, v34, s64, v98
	v_med3_f32 v35, v35, s64, v98
	v_med3_f32 v36, v36, s64, v98
	v_med3_f32 v37, v37, s64, v98
	v_med3_f32 v38, v38, s64, v98
	v_med3_f32 v39, v39, s64, v98
	v_med3_f32 v40, v40, s64, v98
	v_med3_f32 v41, v41, s64, v98
	v_med3_f32 v42, v42, s64, v98
	v_med3_f32 v43, v43, s64, v98
	v_med3_f32 v44, v44, s64, v98
	v_med3_f32 v45, v45, s64, v98
	v_med3_f32 v46, v46, s64, v98
	v_med3_f32 v47, v47, s64, v98
	v_med3_f32 v48, v48, s64, v98
	v_med3_f32 v49, v49, s64, v98
	v_med3_f32 v50, v50, s64, v98
	v_med3_f32 v51, v51, s64, v98
	v_med3_f32 v52, v52, s64, v98
	v_med3_f32 v53, v53, s64, v98
	v_med3_f32 v54, v54, s64, v98
	v_med3_f32 v55, v55, s64, v98
	v_med3_f32 v56, v56, s64, v98
	v_med3_f32 v57, v57, s64, v98
	v_med3_f32 v58, v58, s64, v98
	v_med3_f32 v59, v59, s64, v98
	v_med3_f32 v60, v60, s64, v98
	v_med3_f32 v61, v61, s64, v98
	v_med3_f32 v62, v62, s64, v98
	v_med3_f32 v63, v63, s64, v98
	v_med3_f32 v64, v64, s64, v98
	v_med3_f32 v65, v65, s64, v98
	v_cvt_pk_fp8_f32 v148, v34, v38
	v_cvt_pk_fp8_f32 v149, v50, v54
	v_cvt_pk_fp8_f32 v152, v35, v39
	v_cvt_pk_fp8_f32 v153, v51, v55
	v_cvt_pk_fp8_f32 v158, v36, v40
	v_cvt_pk_fp8_f32 v159, v52, v56
	v_cvt_pk_fp8_f32 v196, v37, v41
	v_cvt_pk_fp8_f32 v197, v53, v57
	v_cvt_pk_fp8_f32 v148, v42, v46 op_sel:[0,0,1]
	v_cvt_pk_fp8_f32 v149, v58, v62 op_sel:[0,0,1]
	v_cvt_pk_fp8_f32 v152, v43, v47 op_sel:[0,0,1]
	v_cvt_pk_fp8_f32 v153, v59, v63 op_sel:[0,0,1]
	v_cvt_pk_fp8_f32 v158, v44, v48 op_sel:[0,0,1]
	v_cvt_pk_fp8_f32 v159, v60, v64 op_sel:[0,0,1]
	v_cvt_pk_fp8_f32 v196, v45, v49 op_sel:[0,0,1]
	v_cvt_pk_fp8_f32 v197, v61, v65 op_sel:[0,0,1]
	s_nop 1
	global_store_dwordx2 v27, v[148:149], s[52:53]
	global_store_dwordx2 v32, v[152:153], s[52:53]
	global_store_dwordx2 v92, v[158:159], s[52:53]
	global_store_dwordx2 v94, v[196:197], s[52:53]
	s_branch .Lcv398_p8_end

.Lcv398_p8_end:
	ds_read_b128 v[34:37], v146 offset:0
	ds_read_b128 v[38:41], v146 offset:1024
	ds_read_b128 v[42:45], v146 offset:2048
	ds_read_b128 v[46:49], v146 offset:3072
	ds_read_b128 v[50:53], v146 offset:4096
	ds_read_b128 v[54:57], v146 offset:5120
	ds_read_b128 v[58:61], v146 offset:6144
	ds_read_b128 v[62:65], v146 offset:7168
	s_waitcnt lgkmcnt(0)
	s_lshl_b32 s60, s65, 2
	v_mul_lo_u32 v27, v97, s60
	s_cmp_eq_u32 s71, 0
	s_cbranch_scc1 .Lcv398_p9_bf
	v_lshl_add_u32 v27, v96, 3, v27
	v_add_u32_e32 v32, s65, v27
	v_add_u32_e32 v92, s65, v32
	v_add_u32_e32 v94, s65, v92
	v_mul_f32_e32 v34, s71, v34
	v_mul_f32_e32 v35, s71, v35
	v_mul_f32_e32 v36, s71, v36
	v_mul_f32_e32 v37, s71, v37
	v_mul_f32_e32 v38, s71, v38
	v_mul_f32_e32 v39, s71, v39
	v_mul_f32_e32 v40, s71, v40
	v_mul_f32_e32 v41, s71, v41
	v_mul_f32_e32 v42, s71, v42
	v_mul_f32_e32 v43, s71, v43
	v_mul_f32_e32 v44, s71, v44
	v_mul_f32_e32 v45, s71, v45
	v_mul_f32_e32 v46, s71, v46
	v_mul_f32_e32 v47, s71, v47
	v_mul_f32_e32 v48, s71, v48
	v_mul_f32_e32 v49, s71, v49
	v_mul_f32_e32 v50, s71, v50
	v_mul_f32_e32 v51, s71, v51
	v_mul_f32_e32 v52, s71, v52
	v_mul_f32_e32 v53, s71, v53
	v_mul_f32_e32 v54, s71, v54
	v_mul_f32_e32 v55, s71, v55
	v_mul_f32_e32 v56, s71, v56
	v_mul_f32_e32 v57, s71, v57
	v_mul_f32_e32 v58, s71, v58
	v_mul_f32_e32 v59, s71, v59
	v_mul_f32_e32 v60, s71, v60
	v_mul_f32_e32 v61, s71, v61
	v_mul_f32_e32 v62, s71, v62
	v_mul_f32_e32 v63, s71, v63
	v_mul_f32_e32 v64, s71, v64
	v_mul_f32_e32 v65, s71, v65
	v_med3_f32 v34, v34, s64, v98
	v_med3_f32 v35, v35, s64, v98
	v_med3_f32 v36, v36, s64, v98
	v_med3_f32 v37, v37, s64, v98
	v_med3_f32 v38, v38, s64, v98
	v_med3_f32 v39, v39, s64, v98
	v_med3_f32 v40, v40, s64, v98
	v_med3_f32 v41, v41, s64, v98
	v_med3_f32 v42, v42, s64, v98
	v_med3_f32 v43, v43, s64, v98
	v_med3_f32 v44, v44, s64, v98
	v_med3_f32 v45, v45, s64, v98
	v_med3_f32 v46, v46, s64, v98
	v_med3_f32 v47, v47, s64, v98
	v_med3_f32 v48, v48, s64, v98
	v_med3_f32 v49, v49, s64, v98
	v_med3_f32 v50, v50, s64, v98
	v_med3_f32 v51, v51, s64, v98
	v_med3_f32 v52, v52, s64, v98
	v_med3_f32 v53, v53, s64, v98
	v_med3_f32 v54, v54, s64, v98
	v_med3_f32 v55, v55, s64, v98
	v_med3_f32 v56, v56, s64, v98
	v_med3_f32 v57, v57, s64, v98
	v_med3_f32 v58, v58, s64, v98
	v_med3_f32 v59, v59, s64, v98
	v_med3_f32 v60, v60, s64, v98
	v_med3_f32 v61, v61, s64, v98
	v_med3_f32 v62, v62, s64, v98
	v_med3_f32 v63, v63, s64, v98
	v_med3_f32 v64, v64, s64, v98
	v_med3_f32 v65, v65, s64, v98
	v_cvt_pk_fp8_f32 v148, v34, v38
	v_cvt_pk_fp8_f32 v149, v50, v54
	v_cvt_pk_fp8_f32 v152, v35, v39
	v_cvt_pk_fp8_f32 v153, v51, v55
	v_cvt_pk_fp8_f32 v158, v36, v40
	v_cvt_pk_fp8_f32 v159, v52, v56
	v_cvt_pk_fp8_f32 v196, v37, v41
	v_cvt_pk_fp8_f32 v197, v53, v57
	v_cvt_pk_fp8_f32 v148, v42, v46 op_sel:[0,0,1]
	v_cvt_pk_fp8_f32 v149, v58, v62 op_sel:[0,0,1]
	v_cvt_pk_fp8_f32 v152, v43, v47 op_sel:[0,0,1]
	v_cvt_pk_fp8_f32 v153, v59, v63 op_sel:[0,0,1]
	v_cvt_pk_fp8_f32 v158, v44, v48 op_sel:[0,0,1]
	v_cvt_pk_fp8_f32 v159, v60, v64 op_sel:[0,0,1]
	v_cvt_pk_fp8_f32 v196, v45, v49 op_sel:[0,0,1]
	v_cvt_pk_fp8_f32 v197, v61, v65 op_sel:[0,0,1]
	s_nop 1
	global_store_dwordx2 v27, v[148:149], s[50:51]
	global_store_dwordx2 v32, v[152:153], s[50:51]
	global_store_dwordx2 v92, v[158:159], s[50:51]
	global_store_dwordx2 v94, v[196:197], s[50:51]
	s_branch .Lcv398_p9_end

.Lcv398_drain:
	s_waitcnt vmcnt(0)
	s_cmp_gt_u32 s41, 0
	s_cbranch_scc0 .Lcv398_done
	ds_read_b128 v[34:37], v146 offset:0
	ds_read_b128 v[38:41], v146 offset:1024
	ds_read_b128 v[42:45], v146 offset:2048
	ds_read_b128 v[46:49], v146 offset:3072
	ds_read_b128 v[50:53], v146 offset:4096
	ds_read_b128 v[54:57], v146 offset:5120
	ds_read_b128 v[58:61], v146 offset:6144
	ds_read_b128 v[62:65], v146 offset:7168
	s_waitcnt lgkmcnt(0)
	s_lshl_b32 s60, s65, 2
	v_mul_lo_u32 v27, v97, s60
	s_cmp_eq_u32 s71, 0
	s_cbranch_scc1 .Lcv398_p10_bf
	v_lshl_add_u32 v27, v96, 3, v27
	v_add_u32_e32 v32, s65, v27
	v_add_u32_e32 v92, s65, v32
	v_add_u32_e32 v94, s65, v92
	v_mul_f32_e32 v34, s71, v34
	v_mul_f32_e32 v35, s71, v35
	v_mul_f32_e32 v36, s71, v36
	v_mul_f32_e32 v37, s71, v37
	v_mul_f32_e32 v38, s71, v38
	v_mul_f32_e32 v39, s71, v39
	v_mul_f32_e32 v40, s71, v40
	v_mul_f32_e32 v41, s71, v41
	v_mul_f32_e32 v42, s71, v42
	v_mul_f32_e32 v43, s71, v43
	v_mul_f32_e32 v44, s71, v44
	v_mul_f32_e32 v45, s71, v45
	v_mul_f32_e32 v46, s71, v46
	v_mul_f32_e32 v47, s71, v47
	v_mul_f32_e32 v48, s71, v48
	v_mul_f32_e32 v49, s71, v49
	v_mul_f32_e32 v50, s71, v50
	v_mul_f32_e32 v51, s71, v51
	v_mul_f32_e32 v52, s71, v52
	v_mul_f32_e32 v53, s71, v53
	v_mul_f32_e32 v54, s71, v54
	v_mul_f32_e32 v55, s71, v55
	v_mul_f32_e32 v56, s71, v56
	v_mul_f32_e32 v57, s71, v57
	v_mul_f32_e32 v58, s71, v58
	v_mul_f32_e32 v59, s71, v59
	v_mul_f32_e32 v60, s71, v60
	v_mul_f32_e32 v61, s71, v61
	v_mul_f32_e32 v62, s71, v62
	v_mul_f32_e32 v63, s71, v63
	v_mul_f32_e32 v64, s71, v64
	v_mul_f32_e32 v65, s71, v65
	v_med3_f32 v34, v34, s64, v98
	v_med3_f32 v35, v35, s64, v98
	v_med3_f32 v36, v36, s64, v98
	v_med3_f32 v37, v37, s64, v98
	v_med3_f32 v38, v38, s64, v98
	v_med3_f32 v39, v39, s64, v98
	v_med3_f32 v40, v40, s64, v98
	v_med3_f32 v41, v41, s64, v98
	v_med3_f32 v42, v42, s64, v98
	v_med3_f32 v43, v43, s64, v98
	v_med3_f32 v44, v44, s64, v98
	v_med3_f32 v45, v45, s64, v98
	v_med3_f32 v46, v46, s64, v98
	v_med3_f32 v47, v47, s64, v98
	v_med3_f32 v48, v48, s64, v98
	v_med3_f32 v49, v49, s64, v98
	v_med3_f32 v50, v50, s64, v98
	v_med3_f32 v51, v51, s64, v98
	v_med3_f32 v52, v52, s64, v98
	v_med3_f32 v53, v53, s64, v98
	v_med3_f32 v54, v54, s64, v98
	v_med3_f32 v55, v55, s64, v98
	v_med3_f32 v56, v56, s64, v98
	v_med3_f32 v57, v57, s64, v98
	v_med3_f32 v58, v58, s64, v98
	v_med3_f32 v59, v59, s64, v98
	v_med3_f32 v60, v60, s64, v98
	v_med3_f32 v61, v61, s64, v98
	v_med3_f32 v62, v62, s64, v98
	v_med3_f32 v63, v63, s64, v98
	v_med3_f32 v64, v64, s64, v98
	v_med3_f32 v65, v65, s64, v98
	v_cvt_pk_fp8_f32 v148, v34, v38
	v_cvt_pk_fp8_f32 v149, v50, v54
	v_cvt_pk_fp8_f32 v152, v35, v39
	v_cvt_pk_fp8_f32 v153, v51, v55
	v_cvt_pk_fp8_f32 v158, v36, v40
	v_cvt_pk_fp8_f32 v159, v52, v56
	v_cvt_pk_fp8_f32 v196, v37, v41
	v_cvt_pk_fp8_f32 v197, v53, v57
	v_cvt_pk_fp8_f32 v148, v42, v46 op_sel:[0,0,1]
	v_cvt_pk_fp8_f32 v149, v58, v62 op_sel:[0,0,1]
	v_cvt_pk_fp8_f32 v152, v43, v47 op_sel:[0,0,1]
	v_cvt_pk_fp8_f32 v153, v59, v63 op_sel:[0,0,1]
	v_cvt_pk_fp8_f32 v158, v44, v48 op_sel:[0,0,1]
	v_cvt_pk_fp8_f32 v159, v60, v64 op_sel:[0,0,1]
	v_cvt_pk_fp8_f32 v196, v45, v49 op_sel:[0,0,1]
	v_cvt_pk_fp8_f32 v197, v61, v65 op_sel:[0,0,1]
	s_nop 1
	global_store_dwordx2 v27, v[148:149], s[50:51]
	global_store_dwordx2 v32, v[152:153], s[50:51]
	global_store_dwordx2 v92, v[158:159], s[50:51]
	global_store_dwordx2 v94, v[196:197], s[50:51]
	s_branch .Lcv398_p10_end

.Lcv398_p10_end:
	s_cmp_gt_u32 s41, 1
	s_cbranch_scc0 .Lcv398_done
	ds_read_b128 v[34:37], v171 offset:0
	ds_read_b128 v[38:41], v171 offset:1024
	ds_read_b128 v[42:45], v171 offset:2048
	ds_read_b128 v[46:49], v171 offset:3072
	ds_read_b128 v[50:53], v171 offset:4096
	ds_read_b128 v[54:57], v171 offset:5120
	ds_read_b128 v[58:61], v171 offset:6144
	ds_read_b128 v[62:65], v171 offset:7168
	s_waitcnt lgkmcnt(0)
	s_lshl_b32 s60, s66, 2
	v_mul_lo_u32 v27, v97, s60
	s_cmp_eq_u32 s75, 0
	s_cbranch_scc1 .Lcv398_p11_bf
	v_lshl_add_u32 v27, v96, 3, v27
	v_add_u32_e32 v32, s66, v27
	v_add_u32_e32 v92, s66, v32
	v_add_u32_e32 v94, s66, v92
	v_mul_f32_e32 v34, s75, v34
	v_mul_f32_e32 v35, s75, v35
	v_mul_f32_e32 v36, s75, v36
	v_mul_f32_e32 v37, s75, v37
	v_mul_f32_e32 v38, s75, v38
	v_mul_f32_e32 v39, s75, v39
	v_mul_f32_e32 v40, s75, v40
	v_mul_f32_e32 v41, s75, v41
	v_mul_f32_e32 v42, s75, v42
	v_mul_f32_e32 v43, s75, v43
	v_mul_f32_e32 v44, s75, v44
	v_mul_f32_e32 v45, s75, v45
	v_mul_f32_e32 v46, s75, v46
	v_mul_f32_e32 v47, s75, v47
	v_mul_f32_e32 v48, s75, v48
	v_mul_f32_e32 v49, s75, v49
	v_mul_f32_e32 v50, s75, v50
	v_mul_f32_e32 v51, s75, v51
	v_mul_f32_e32 v52, s75, v52
	v_mul_f32_e32 v53, s75, v53
	v_mul_f32_e32 v54, s75, v54
	v_mul_f32_e32 v55, s75, v55
	v_mul_f32_e32 v56, s75, v56
	v_mul_f32_e32 v57, s75, v57
	v_mul_f32_e32 v58, s75, v58
	v_mul_f32_e32 v59, s75, v59
	v_mul_f32_e32 v60, s75, v60
	v_mul_f32_e32 v61, s75, v61
	v_mul_f32_e32 v62, s75, v62
	v_mul_f32_e32 v63, s75, v63
	v_mul_f32_e32 v64, s75, v64
	v_mul_f32_e32 v65, s75, v65
	v_med3_f32 v34, v34, s64, v98
	v_med3_f32 v35, v35, s64, v98
	v_med3_f32 v36, v36, s64, v98
	v_med3_f32 v37, v37, s64, v98
	v_med3_f32 v38, v38, s64, v98
	v_med3_f32 v39, v39, s64, v98
	v_med3_f32 v40, v40, s64, v98
	v_med3_f32 v41, v41, s64, v98
	v_med3_f32 v42, v42, s64, v98
	v_med3_f32 v43, v43, s64, v98
	v_med3_f32 v44, v44, s64, v98
	v_med3_f32 v45, v45, s64, v98
	v_med3_f32 v46, v46, s64, v98
	v_med3_f32 v47, v47, s64, v98
	v_med3_f32 v48, v48, s64, v98
	v_med3_f32 v49, v49, s64, v98
	v_med3_f32 v50, v50, s64, v98
	v_med3_f32 v51, v51, s64, v98
	v_med3_f32 v52, v52, s64, v98
	v_med3_f32 v53, v53, s64, v98
	v_med3_f32 v54, v54, s64, v98
	v_med3_f32 v55, v55, s64, v98
	v_med3_f32 v56, v56, s64, v98
	v_med3_f32 v57, v57, s64, v98
	v_med3_f32 v58, v58, s64, v98
	v_med3_f32 v59, v59, s64, v98
	v_med3_f32 v60, v60, s64, v98
	v_med3_f32 v61, v61, s64, v98
	v_med3_f32 v62, v62, s64, v98
	v_med3_f32 v63, v63, s64, v98
	v_med3_f32 v64, v64, s64, v98
	v_med3_f32 v65, v65, s64, v98
	v_cvt_pk_fp8_f32 v148, v34, v38
	v_cvt_pk_fp8_f32 v149, v50, v54
	v_cvt_pk_fp8_f32 v152, v35, v39
	v_cvt_pk_fp8_f32 v153, v51, v55
	v_cvt_pk_fp8_f32 v158, v36, v40
	v_cvt_pk_fp8_f32 v159, v52, v56
	v_cvt_pk_fp8_f32 v196, v37, v41
	v_cvt_pk_fp8_f32 v197, v53, v57
	v_cvt_pk_fp8_f32 v148, v42, v46 op_sel:[0,0,1]
	v_cvt_pk_fp8_f32 v149, v58, v62 op_sel:[0,0,1]
	v_cvt_pk_fp8_f32 v152, v43, v47 op_sel:[0,0,1]
	v_cvt_pk_fp8_f32 v153, v59, v63 op_sel:[0,0,1]
	v_cvt_pk_fp8_f32 v158, v44, v48 op_sel:[0,0,1]
	v_cvt_pk_fp8_f32 v159, v60, v64 op_sel:[0,0,1]
	v_cvt_pk_fp8_f32 v196, v45, v49 op_sel:[0,0,1]
	v_cvt_pk_fp8_f32 v197, v61, v65 op_sel:[0,0,1]
	s_nop 1
	global_store_dwordx2 v27, v[148:149], s[52:53]
	global_store_dwordx2 v32, v[152:153], s[52:53]
	global_store_dwordx2 v92, v[158:159], s[52:53]
	global_store_dwordx2 v94, v[196:197], s[52:53]
	s_branch .Lcv398_p11_end

.Lcv398_p11_end:
.Lcv398_done:
	s_waitcnt vmcnt(0) lgkmcnt(0)

.Lcvt_site_1333:
	s_waitcnt vmcnt(0) lgkmcnt(0)
	v_readlane_b32 s0, v254, 42
	v_readlane_b32 s1, v254, 43
	v_readlane_b32 s60, v254, 0
	v_readlane_b32 s61, v254, 41
	s_nop 3
	s_sub_u32 s0, s0, 0xd0
	s_subb_u32 s1, s1, 0
	s_load_dwordx2 s[10:11], s[0:1], 0x38
	s_load_dwordx2 s[12:13], s[0:1], 0x40
	s_load_dwordx2 s[14:15], s[0:1], 0x88
	s_load_dwordx2 s[28:29], s[0:1], 0x90
	s_load_dwordx2 s[38:39], s[0:1], 0x98
	s_load_dwordx2 s[44:45], s[0:1], 0xa0
	s_load_dwordx2 s[46:47], s[0:1], 0xa8
	s_load_dwordx2 s[48:49], s[0:1], 0xb8
	v_mbcnt_lo_u32_b32 v100, -1, 0
	v_mbcnt_hi_u32_b32 v100, -1, v100
	v_and_b32_e32 v96, 7, v100
	v_lshrrev_b32_e32 v97, 3, v100
	v_mov_b32_e32 v98, 0x43e00000
	s_mov_b32 s64, 0xc3e00000
	s_lshl_b32 s9, s60, 3
	s_add_u32 s9, s9, s61
	s_min_u32 s20, s74, 0x80
	s_lshl_b32 s20, s20, 4
	s_lshl_b32 s79, s61, 14
	s_add_u32 s69, s79, 0x2000
	v_lshlrev_b32_e32 v146, 4, v100
	v_add_u32_e32 v171, s69, v146
	v_add_u32_e32 v146, s79, v146
	s_waitcnt lgkmcnt(0)
	s_add_u32 s14, s14, 0x8000000
	s_addc_u32 s15, s15, 0
	s_add_u32 s28, s28, 0x8000000
	s_addc_u32 s29, s29, 0
	s_add_u32 s38, s38, 0x8000000
	s_addc_u32 s39, s39, 0
	s_add_u32 s44, s44, 0x800000
	s_addc_u32 s45, s45, 0
	s_add_u32 s46, s46, 0x200000
	s_addc_u32 s47, s47, 0
	s_lshl_b32 s32, s9, 1
	s_mov_b32 s41, 0
	s_cmp_lt_u32 s32, 0x6a80
	s_cbranch_scc0 .Lcv1333_drain
	s_add_u32 s43, s32, 0
	s_cmp_lt_u32 s43, 0x600
	s_cbranch_scc0 .Lcv1333_d0_b
	s_mul_i32 s58, s43, 0xaaab
	s_lshr_b32 s58, s58, 22
	s_mul_i32 s59, s58, 96
	s_sub_u32 s59, s43, s59
	s_mul_i32 s60, s58, 0xc0000
	s_mul_i32 s81, s59, 0x80
	s_add_u32 s60, s60, s81
	s_add_u32 s2, s10, s60
	s_addc_u32 s3, s11, 0
	s_mov_b32 s63, 0x3000
	s_mul_i32 s61, s59, 0x8000
	s_mul_i32 s81, s58, 0x40
	s_add_u32 s61, s61, s81
	s_add_u32 s61, s61, 0x800000
	s_add_u32 s50, s48, s61
	s_addc_u32 s51, s49, 0
	s_mov_b32 s65, 0x400
	s_mov_b32 s71, 0x44000000
	s_branch .Lcv1333_d0_ld

.Lcv1333_d0_ld:
	s_lshl_b32 s60, s63, 3
	v_mul_lo_u32 v0, v96, s60
	v_lshl_add_u32 v0, v97, 4, v0
	v_add_u32_e32 v4, s63, v0
	v_add_u32_e32 v10, s63, v4
	v_add_u32_e32 v11, s63, v10
	v_add_u32_e32 v12, s63, v11
	v_add_u32_e32 v19, s63, v12
	v_add_u32_e32 v24, s63, v19
	v_add_u32_e32 v25, s63, v24
	s_add_i32 m0, s79, 0x0
	s_nop 0
	global_load_lds_dwordx4 v0, s[2:3] nt
	s_add_i32 m0, s79, 0x400
	s_nop 0
	global_load_lds_dwordx4 v4, s[2:3] nt
	s_add_i32 m0, s79, 0x800
	s_nop 0
	global_load_lds_dwordx4 v10, s[2:3] nt
	s_add_i32 m0, s79, 0xc00
	s_nop 0
	global_load_lds_dwordx4 v11, s[2:3] nt
	s_add_i32 m0, s79, 0x1000
	s_nop 0
	global_load_lds_dwordx4 v12, s[2:3] nt
	s_add_i32 m0, s79, 0x1400
	s_nop 0
	global_load_lds_dwordx4 v19, s[2:3] nt
	s_add_i32 m0, s79, 0x1800
	s_nop 0
	global_load_lds_dwordx4 v24, s[2:3] nt
	s_add_i32 m0, s79, 0x1c00
	s_nop 0
	global_load_lds_dwordx4 v25, s[2:3] nt
	s_mov_b32 s41, 1
	s_cmp_lt_u32 s32, 0x6a80
	s_cbranch_scc0 .Lcv1333_drain
	s_add_u32 s43, s32, 1
	s_cmp_lt_u32 s43, 0x600
	s_cbranch_scc0 .Lcv1333_d1_b
	s_mul_i32 s58, s43, 0xaaab
	s_lshr_b32 s58, s58, 22
	s_mul_i32 s59, s58, 96
	s_sub_u32 s59, s43, s59
	s_mul_i32 s60, s58, 0xc0000
	s_mul_i32 s81, s59, 0x80
	s_add_u32 s60, s60, s81
	s_add_u32 s2, s10, s60
	s_addc_u32 s3, s11, 0
	s_mov_b32 s63, 0x3000
	s_mul_i32 s61, s59, 0x8000
	s_mul_i32 s81, s58, 0x40
	s_add_u32 s61, s61, s81
	s_add_u32 s61, s61, 0x800000
	s_add_u32 s52, s48, s61
	s_addc_u32 s53, s49, 0
	s_mov_b32 s66, 0x400
	s_mov_b32 s75, 0x44000000
	s_branch .Lcv1333_d1_ld

.Lcv1333_loop:
	s_cmp_lt_u32 s32, 0x6a80
	s_cbranch_scc0 .Lcv1333_drain0
	s_waitcnt vmcnt(8)
	ds_read_b128 v[34:37], v146 offset:0
	ds_read_b128 v[38:41], v146 offset:1024
	ds_read_b128 v[42:45], v146 offset:2048
	ds_read_b128 v[46:49], v146 offset:3072
	ds_read_b128 v[50:53], v146 offset:4096
	ds_read_b128 v[54:57], v146 offset:5120
	ds_read_b128 v[58:61], v146 offset:6144
	ds_read_b128 v[62:65], v146 offset:7168
	s_waitcnt lgkmcnt(0)
	s_mov_b64 s[2:3], s[50:51]
	s_lshl_b32 s60, s65, 2
	v_mul_lo_u32 v27, v97, s60
	s_cmp_eq_u32 s71, 0
	s_cbranch_scc1 .Lcv1333_p2_bf
	v_lshl_add_u32 v27, v96, 3, v27
	v_add_u32_e32 v32, s65, v27
	v_add_u32_e32 v92, s65, v32
	v_add_u32_e32 v94, s65, v92
	v_mul_f32_e32 v34, s71, v34
	v_mul_f32_e32 v35, s71, v35
	v_mul_f32_e32 v36, s71, v36
	v_mul_f32_e32 v37, s71, v37
	v_mul_f32_e32 v38, s71, v38
	v_mul_f32_e32 v39, s71, v39
	v_mul_f32_e32 v40, s71, v40
	v_mul_f32_e32 v41, s71, v41
	v_mul_f32_e32 v42, s71, v42
	v_mul_f32_e32 v43, s71, v43
	v_mul_f32_e32 v44, s71, v44
	v_mul_f32_e32 v45, s71, v45
	v_mul_f32_e32 v46, s71, v46
	v_mul_f32_e32 v47, s71, v47
	v_mul_f32_e32 v48, s71, v48
	v_mul_f32_e32 v49, s71, v49
	v_mul_f32_e32 v50, s71, v50
	v_mul_f32_e32 v51, s71, v51
	v_mul_f32_e32 v52, s71, v52
	v_mul_f32_e32 v53, s71, v53
	v_mul_f32_e32 v54, s71, v54
	v_mul_f32_e32 v55, s71, v55
	v_mul_f32_e32 v56, s71, v56
	v_mul_f32_e32 v57, s71, v57
	v_mul_f32_e32 v58, s71, v58
	v_mul_f32_e32 v59, s71, v59
	v_mul_f32_e32 v60, s71, v60
	v_mul_f32_e32 v61, s71, v61
	v_mul_f32_e32 v62, s71, v62
	v_mul_f32_e32 v63, s71, v63
	v_mul_f32_e32 v64, s71, v64
	v_mul_f32_e32 v65, s71, v65
	v_med3_f32 v34, v34, s64, v98
	v_med3_f32 v35, v35, s64, v98
	v_med3_f32 v36, v36, s64, v98
	v_med3_f32 v37, v37, s64, v98
	v_med3_f32 v38, v38, s64, v98
	v_med3_f32 v39, v39, s64, v98
	v_med3_f32 v40, v40, s64, v98
	v_med3_f32 v41, v41, s64, v98
	v_med3_f32 v42, v42, s64, v98
	v_med3_f32 v43, v43, s64, v98
	v_med3_f32 v44, v44, s64, v98
	v_med3_f32 v45, v45, s64, v98
	v_med3_f32 v46, v46, s64, v98
	v_med3_f32 v47, v47, s64, v98
	v_med3_f32 v48, v48, s64, v98
	v_med3_f32 v49, v49, s64, v98
	v_med3_f32 v50, v50, s64, v98
	v_med3_f32 v51, v51, s64, v98
	v_med3_f32 v52, v52, s64, v98
	v_med3_f32 v53, v53, s64, v98
	v_med3_f32 v54, v54, s64, v98
	v_med3_f32 v55, v55, s64, v98
	v_med3_f32 v56, v56, s64, v98
	v_med3_f32 v57, v57, s64, v98
	v_med3_f32 v58, v58, s64, v98
	v_med3_f32 v59, v59, s64, v98
	v_med3_f32 v60, v60, s64, v98
	v_med3_f32 v61, v61, s64, v98
	v_med3_f32 v62, v62, s64, v98
	v_med3_f32 v63, v63, s64, v98
	v_med3_f32 v64, v64, s64, v98
	v_med3_f32 v65, v65, s64, v98
	v_cvt_pk_fp8_f32 v148, v34, v38
	v_cvt_pk_fp8_f32 v149, v50, v54
	v_cvt_pk_fp8_f32 v152, v35, v39
	v_cvt_pk_fp8_f32 v153, v51, v55
	v_cvt_pk_fp8_f32 v158, v36, v40
	v_cvt_pk_fp8_f32 v159, v52, v56
	v_cvt_pk_fp8_f32 v196, v37, v41
	v_cvt_pk_fp8_f32 v197, v53, v57
	v_cvt_pk_fp8_f32 v148, v42, v46 op_sel:[0,0,1]
	v_cvt_pk_fp8_f32 v149, v58, v62 op_sel:[0,0,1]
	v_cvt_pk_fp8_f32 v152, v43, v47 op_sel:[0,0,1]
	v_cvt_pk_fp8_f32 v153, v59, v63 op_sel:[0,0,1]
	v_cvt_pk_fp8_f32 v158, v44, v48 op_sel:[0,0,1]
	v_cvt_pk_fp8_f32 v159, v60, v64 op_sel:[0,0,1]
	v_cvt_pk_fp8_f32 v196, v45, v49 op_sel:[0,0,1]
	v_cvt_pk_fp8_f32 v197, v61, v65 op_sel:[0,0,1]
	s_nop 1
	global_store_dwordx2 v27, v[148:149], s[50:51]
	global_store_dwordx2 v32, v[152:153], s[50:51]
	global_store_dwordx2 v92, v[158:159], s[50:51]
	global_store_dwordx2 v94, v[196:197], s[50:51]
	s_branch .Lcv1333_p2_end

.Lcv1333_d3_ld:
	s_lshl_b32 s60, s63, 3
	v_mul_lo_u32 v0, v96, s60
	v_lshl_add_u32 v0, v97, 4, v0
	v_add_u32_e32 v4, s63, v0
	v_add_u32_e32 v10, s63, v4
	v_add_u32_e32 v11, s63, v10
	v_add_u32_e32 v12, s63, v11
	v_add_u32_e32 v19, s63, v12
	v_add_u32_e32 v24, s63, v19
	v_add_u32_e32 v25, s63, v24
	s_add_i32 m0, s79, 0x0
	s_nop 0
	global_load_lds_dwordx4 v0, s[2:3] nt
	s_add_i32 m0, s79, 0x400
	s_nop 0
	global_load_lds_dwordx4 v4, s[2:3] nt
	s_add_i32 m0, s79, 0x800
	s_nop 0
	global_load_lds_dwordx4 v10, s[2:3] nt
	s_add_i32 m0, s79, 0xc00
	s_nop 0
	global_load_lds_dwordx4 v11, s[2:3] nt
	s_add_i32 m0, s79, 0x1000
	s_nop 0
	global_load_lds_dwordx4 v12, s[2:3] nt
	s_add_i32 m0, s79, 0x1400
	s_nop 0
	global_load_lds_dwordx4 v19, s[2:3] nt
	s_add_i32 m0, s79, 0x1800
	s_nop 0
	global_load_lds_dwordx4 v24, s[2:3] nt
	s_add_i32 m0, s79, 0x1c00
	s_nop 0
	global_load_lds_dwordx4 v25, s[2:3] nt
	s_cmp_lt_u32 s32, 0x6a80
	s_cbranch_scc0 .Lcv1333_drain1
	s_waitcnt vmcnt(8)
	ds_read_b128 v[34:37], v171 offset:0
	ds_read_b128 v[38:41], v171 offset:1024
	ds_read_b128 v[42:45], v171 offset:2048
	ds_read_b128 v[46:49], v171 offset:3072
	ds_read_b128 v[50:53], v171 offset:4096
	ds_read_b128 v[54:57], v171 offset:5120
	ds_read_b128 v[58:61], v171 offset:6144
	ds_read_b128 v[62:65], v171 offset:7168
	s_waitcnt lgkmcnt(0)
	s_mov_b64 s[2:3], s[52:53]
	s_lshl_b32 s60, s66, 2
	v_mul_lo_u32 v27, v97, s60
	s_cmp_eq_u32 s75, 0
	s_cbranch_scc1 .Lcv1333_p4_bf
	v_lshl_add_u32 v27, v96, 3, v27
	v_add_u32_e32 v32, s66, v27
	v_add_u32_e32 v92, s66, v32
	v_add_u32_e32 v94, s66, v92
	v_mul_f32_e32 v34, s75, v34
	v_mul_f32_e32 v35, s75, v35
	v_mul_f32_e32 v36, s75, v36
	v_mul_f32_e32 v37, s75, v37
	v_mul_f32_e32 v38, s75, v38
	v_mul_f32_e32 v39, s75, v39
	v_mul_f32_e32 v40, s75, v40
	v_mul_f32_e32 v41, s75, v41
	v_mul_f32_e32 v42, s75, v42
	v_mul_f32_e32 v43, s75, v43
	v_mul_f32_e32 v44, s75, v44
	v_mul_f32_e32 v45, s75, v45
	v_mul_f32_e32 v46, s75, v46
	v_mul_f32_e32 v47, s75, v47
	v_mul_f32_e32 v48, s75, v48
	v_mul_f32_e32 v49, s75, v49
	v_mul_f32_e32 v50, s75, v50
	v_mul_f32_e32 v51, s75, v51
	v_mul_f32_e32 v52, s75, v52
	v_mul_f32_e32 v53, s75, v53
	v_mul_f32_e32 v54, s75, v54
	v_mul_f32_e32 v55, s75, v55
	v_mul_f32_e32 v56, s75, v56
	v_mul_f32_e32 v57, s75, v57
	v_mul_f32_e32 v58, s75, v58
	v_mul_f32_e32 v59, s75, v59
	v_mul_f32_e32 v60, s75, v60
	v_mul_f32_e32 v61, s75, v61
	v_mul_f32_e32 v62, s75, v62
	v_mul_f32_e32 v63, s75, v63
	v_mul_f32_e32 v64, s75, v64
	v_mul_f32_e32 v65, s75, v65
	v_med3_f32 v34, v34, s64, v98
	v_med3_f32 v35, v35, s64, v98
	v_med3_f32 v36, v36, s64, v98
	v_med3_f32 v37, v37, s64, v98
	v_med3_f32 v38, v38, s64, v98
	v_med3_f32 v39, v39, s64, v98
	v_med3_f32 v40, v40, s64, v98
	v_med3_f32 v41, v41, s64, v98
	v_med3_f32 v42, v42, s64, v98
	v_med3_f32 v43, v43, s64, v98
	v_med3_f32 v44, v44, s64, v98
	v_med3_f32 v45, v45, s64, v98
	v_med3_f32 v46, v46, s64, v98
	v_med3_f32 v47, v47, s64, v98
	v_med3_f32 v48, v48, s64, v98
	v_med3_f32 v49, v49, s64, v98
	v_med3_f32 v50, v50, s64, v98
	v_med3_f32 v51, v51, s64, v98
	v_med3_f32 v52, v52, s64, v98
	v_med3_f32 v53, v53, s64, v98
	v_med3_f32 v54, v54, s64, v98
	v_med3_f32 v55, v55, s64, v98
	v_med3_f32 v56, v56, s64, v98
	v_med3_f32 v57, v57, s64, v98
	v_med3_f32 v58, v58, s64, v98
	v_med3_f32 v59, v59, s64, v98
	v_med3_f32 v60, v60, s64, v98
	v_med3_f32 v61, v61, s64, v98
	v_med3_f32 v62, v62, s64, v98
	v_med3_f32 v63, v63, s64, v98
	v_med3_f32 v64, v64, s64, v98
	v_med3_f32 v65, v65, s64, v98
	v_cvt_pk_fp8_f32 v148, v34, v38
	v_cvt_pk_fp8_f32 v149, v50, v54
	v_cvt_pk_fp8_f32 v152, v35, v39
	v_cvt_pk_fp8_f32 v153, v51, v55
	v_cvt_pk_fp8_f32 v158, v36, v40
	v_cvt_pk_fp8_f32 v159, v52, v56
	v_cvt_pk_fp8_f32 v196, v37, v41
	v_cvt_pk_fp8_f32 v197, v53, v57
	v_cvt_pk_fp8_f32 v148, v42, v46 op_sel:[0,0,1]
	v_cvt_pk_fp8_f32 v149, v58, v62 op_sel:[0,0,1]
	v_cvt_pk_fp8_f32 v152, v43, v47 op_sel:[0,0,1]
	v_cvt_pk_fp8_f32 v153, v59, v63 op_sel:[0,0,1]
	v_cvt_pk_fp8_f32 v158, v44, v48 op_sel:[0,0,1]
	v_cvt_pk_fp8_f32 v159, v60, v64 op_sel:[0,0,1]
	v_cvt_pk_fp8_f32 v196, v45, v49 op_sel:[0,0,1]
	v_cvt_pk_fp8_f32 v197, v61, v65 op_sel:[0,0,1]
	s_nop 1
	global_store_dwordx2 v27, v[148:149], s[52:53]
	global_store_dwordx2 v32, v[152:153], s[52:53]
	global_store_dwordx2 v92, v[158:159], s[52:53]
	global_store_dwordx2 v94, v[196:197], s[52:53]
	s_branch .Lcv1333_p4_end

.Lcvt_site_2210:
	s_waitcnt vmcnt(0) lgkmcnt(0)
	v_readlane_b32 s0, v254, 42
	v_readlane_b32 s1, v254, 43
	v_readlane_b32 s60, v254, 0
	v_readlane_b32 s61, v254, 41
	s_nop 3
	s_sub_u32 s0, s0, 0xd0
	s_subb_u32 s1, s1, 0
	s_load_dwordx2 s[10:11], s[0:1], 0x10
	s_load_dwordx2 s[12:13], s[0:1], 0x18
	s_load_dwordx2 s[14:15], s[0:1], 0x88
	s_load_dwordx2 s[28:29], s[0:1], 0x90
	s_load_dwordx2 s[38:39], s[0:1], 0x98
	s_load_dwordx2 s[44:45], s[0:1], 0xa0
	s_load_dwordx2 s[46:47], s[0:1], 0xa8
	s_load_dwordx2 s[48:49], s[0:1], 0xb8
	v_mbcnt_lo_u32_b32 v100, -1, 0
	v_mbcnt_hi_u32_b32 v100, -1, v100
	v_and_b32_e32 v96, 7, v100
	v_lshrrev_b32_e32 v97, 3, v100
	v_mov_b32_e32 v98, 0x43e00000
	s_mov_b32 s64, 0xc3e00000
	s_lshl_b32 s9, s60, 3
	s_add_u32 s9, s9, s61
	s_min_u32 s20, s74, 0x40
	s_lshl_b32 s20, s20, 4
	s_lshl_b32 s79, s61, 14
	s_add_u32 s69, s79, 0x2000
	v_lshlrev_b32_e32 v146, 4, v100
	v_add_u32_e32 v171, s69, v146
	v_add_u32_e32 v146, s79, v146
	s_waitcnt lgkmcnt(0)
	s_add_u32 s10, s10, 0xc00000
	s_addc_u32 s11, s11, 0
	s_add_u32 s12, s12, 0x400000
	s_addc_u32 s13, s13, 0
	s_add_u32 s14, s14, 0xc000000
	s_addc_u32 s15, s15, 0
	s_add_u32 s28, s28, 0xc000000
	s_addc_u32 s29, s29, 0
	s_add_u32 s38, s38, 0xc000000
	s_addc_u32 s39, s39, 0
	s_add_u32 s44, s44, 0xc00000
	s_addc_u32 s45, s45, 0
	s_add_u32 s46, s46, 0x300000
	s_addc_u32 s47, s47, 0
	s_add_u32 s48, s48, 0x2bd00000
	s_addc_u32 s49, s49, 0
	s_lshl_b32 s32, s9, 1
	s_mov_b32 s41, 0
	s_cmp_lt_u32 s32, 0x6a80
	s_cbranch_scc0 .Lcv2210_drain
	s_add_u32 s43, s32, 0
	s_cmp_lt_u32 s43, 0x600
	s_cbranch_scc0 .Lcv2210_d0_b
	s_mul_i32 s58, s43, 0xaaab
	s_lshr_b32 s58, s58, 22
	s_mul_i32 s59, s58, 96
	s_sub_u32 s59, s43, s59
	s_mul_i32 s60, s58, 0xc0000
	s_mul_i32 s81, s59, 0x80
	s_add_u32 s60, s60, s81
	s_add_u32 s2, s10, s60
	s_addc_u32 s3, s11, 0
	s_mov_b32 s63, 0x3000
	s_mul_i32 s61, s59, 0x8000
	s_mul_i32 s81, s58, 0x40
	s_add_u32 s61, s61, s81
	s_add_u32 s61, s61, 0x800000
	s_add_u32 s50, s48, s61
	s_addc_u32 s51, s49, 0
	s_mov_b32 s65, 0x400
	s_mov_b32 s71, 0x44000000
	s_branch .Lcv2210_d0_ld
